# each scan sequence split over two CUs (32 state columns per MFMA wave, 2 MFMA waves per CU): halves the LDS fragment reads per CU
# speedup vs baseline: 1.0086x; 1.0086x over previous
; DI void gdn_scan_seq(const Params& p, int bh16, char* ldsf) {
;     ...
;   f32x16 S[4];
; #pragma unroll
;   for (int m = 0; m < 4; ++m)
; #pragma unroll
;     for (int r = 0; r < 16; ++r) S[m][r] = 0.f;
;   asm volatile("s_waitcnt vmcnt(0)" ::: "memory");
;   __syncthreads();
;   SCAN_ISSUE(0, 0); SCAN_ISSUE(1, 1);
; DI void phase_mixer(const Params& p, int bid, int nb, char* lds, char* ctl, char* ldsf) {
;     ...
;   if (bid < 32) { if (vb == 0) gdn_scan_seq(p, bid >> 1, ldsf); else { __syncthreads(); for (int k = 0; k < 128; ++k) { __builtin_amdgcn_s_barrier(); asm volatile("" ::: "memory"); } __syncthreads(); } }
.LBB0_1207:
	s_or_b64 exec, exec, s[0:1]
	v_mov_b32_e32 v135, v206
	s_waitcnt lgkmcnt(0)
	s_barrier
	v_cmp_gt_i32_e64 s[6:7], 64, v176
	s_nop 3
	s_and_saveexec_b64 s[0:1], s[6:7]
	s_cbranch_execz .LBB0_1227
	s_movk_i32 s2, 0xff
	v_cmp_lt_u32_e32 vcc, s2, v207
	s_and_saveexec_b64 s[2:3], vcc
	s_xor_b64 s[6:7], exec, s[2:3]
	s_cbranch_execz .LBB0_1212
	v_readlane_b32 s2, v250, 0
	v_lshrrev_b32_e32 v209, 6, v206
	v_and_b32_e32 v208, 63, v206
	v_lshlrev_b32_e32 v132, 12, v209
	v_lshl_or_b32 v132, v208, 4, v132
	v_readfirstlane_b32 s3, v209
	s_nop 3
	s_lshr_b32 s18, s2, 4
	s_and_b32 s2, s2, 15
	s_cmp_lt_u32 s3, 2
	s_cselect_b64 s[16:17], -1, 0
	v_and_b32_e32 v209, 1, v209
	v_lshl_add_u32 v209, s18, 1, v209
	v_lshlrev_b32_e32 v133, 11, v209
	v_lshl_or_b32 v133, v208, 5, v133
	v_add_u32_e32 v134, 0x2000, v133
	v_lshlrev_b32_e32 v210, 12, v209
	v_lshl_or_b32 v210, v208, 4, v210
	v_mov_b32_e32 v208, v132
	s_lshl_b32 s2, s2, 21
	s_add_u32 s8, s84, s2
	s_addc_u32 s9, s85, 0
	s_add_u32 s12, s8, 0x1c000000
	s_addc_u32 s13, s9, 0
	s_add_u32 s8, s8, 0x1e000000
	s_addc_u32 s9, s9, 0
	s_add_u32 s10, s66, s2
	s_addc_u32 s11, s67, 0
	s_add_u32 s10, s10, 0x2000000
	s_addc_u32 s11, s11, 0
	s_mov_b32 s15, 0
	global_load_dwordx4 v[0:3], v132, s[8:9]
	global_load_dwordx4 v[4:7], v132, s[8:9] offset:1024
	global_load_dwordx4 v[8:11], v132, s[8:9] offset:2048
	global_load_dwordx4 v[12:15], v132, s[8:9] offset:3072
	global_load_dwordx4 v[16:19], v132, s[10:11]
	global_load_dwordx4 v[20:23], v132, s[10:11] offset:1024
	global_load_dwordx4 v[24:27], v132, s[10:11] offset:2048
	global_load_dwordx4 v[28:31], v132, s[10:11] offset:3072
	global_load_dwordx4 v[32:35], v133, s[12:13]
	global_load_dwordx4 v[36:39], v133, s[12:13] offset:16
	global_load_dwordx4 v[40:43], v134, s[12:13]
	global_load_dwordx4 v[44:47], v134, s[12:13] offset:16
	s_add_u32 s15, s15, 1
	s_cmp_lt_u32 s15, 0x80
	s_cselect_b32 s14, 0x4000, 0
	s_add_u32 s8, s8, s14
	s_addc_u32 s9, s9, 0
	s_add_u32 s10, s10, s14
	s_addc_u32 s11, s11, 0
	s_add_u32 s12, s12, s14
	s_addc_u32 s13, s13, 0
	global_load_dwordx4 v[48:51], v132, s[8:9]
	global_load_dwordx4 v[52:55], v132, s[8:9] offset:1024
	global_load_dwordx4 v[56:59], v132, s[8:9] offset:2048
	global_load_dwordx4 v[60:63], v132, s[8:9] offset:3072
	global_load_dwordx4 v[64:67], v132, s[10:11]
	global_load_dwordx4 v[68:71], v132, s[10:11] offset:1024
	global_load_dwordx4 v[72:75], v132, s[10:11] offset:2048
	global_load_dwordx4 v[76:79], v132, s[10:11] offset:3072
	global_load_dwordx4 v[80:83], v133, s[12:13]
	global_load_dwordx4 v[84:87], v133, s[12:13] offset:16
	global_load_dwordx4 v[88:91], v134, s[12:13]
	global_load_dwordx4 v[92:95], v134, s[12:13] offset:16
	s_add_u32 s15, s15, 1
	s_cmp_lt_u32 s15, 0x80
	s_cselect_b32 s14, 0x4000, 0
	s_add_u32 s8, s8, s14
	s_addc_u32 s9, s9, 0
	s_add_u32 s10, s10, s14
	s_addc_u32 s11, s11, 0
	s_add_u32 s12, s12, s14
	s_addc_u32 s13, s13, 0
	global_load_dwordx4 v[96:99], v132, s[8:9]
	global_load_dwordx4 v[100:103], v132, s[8:9] offset:1024
	global_load_dwordx4 v[104:107], v132, s[8:9] offset:2048
	global_load_dwordx4 v[108:111], v132, s[8:9] offset:3072
	global_load_dwordx4 v[112:115], v132, s[10:11]
	global_load_dwordx4 v[116:119], v132, s[10:11] offset:1024
	global_load_dwordx4 v[120:123], v132, s[10:11] offset:2048
	global_load_dwordx4 v[124:127], v132, s[10:11] offset:3072
	global_load_dwordx4 v[128:131], v133, s[12:13]
	global_load_dwordx4 v[136:139], v133, s[12:13] offset:16
	global_load_dwordx4 v[140:143], v134, s[12:13]
	global_load_dwordx4 v[148:151], v134, s[12:13] offset:16
	s_add_u32 s15, s15, 1
	s_cmp_lt_u32 s15, 0x80
	s_cselect_b32 s14, 0x4000, 0
	s_add_u32 s8, s8, s14
	s_addc_u32 s9, s9, 0
	s_add_u32 s10, s10, s14
	s_addc_u32 s11, s11, 0
	s_add_u32 s12, s12, s14
	s_addc_u32 s13, s13, 0
	global_load_dwordx4 v[152:155], v132, s[8:9]
	global_load_dwordx4 v[156:159], v132, s[8:9] offset:1024
	global_load_dwordx4 v[160:163], v132, s[8:9] offset:2048
	global_load_dwordx4 v[164:167], v132, s[8:9] offset:3072
	global_load_dwordx4 v[168:171], v132, s[10:11]
	global_load_dwordx4 v[172:175], v132, s[10:11] offset:1024
	global_load_dwordx4 v[178:181], v132, s[10:11] offset:2048
	global_load_dwordx4 v[182:185], v132, s[10:11] offset:3072
	global_load_dwordx4 v[190:193], v133, s[12:13]
	global_load_dwordx4 v[194:197], v133, s[12:13] offset:16
	global_load_dwordx4 v[198:201], v134, s[12:13]
	global_load_dwordx4 v[202:205], v134, s[12:13] offset:16
	s_add_u32 s15, s15, 1
	s_cmp_lt_u32 s15, 0x80
	s_cselect_b32 s14, 0x4000, 0
	s_add_u32 s8, s8, s14
	s_addc_u32 s9, s9, 0
	s_add_u32 s10, s10, s14
	s_addc_u32 s11, s11, 0
	s_add_u32 s12, s12, s14
	s_addc_u32 s13, s13, 0
	s_mov_b32 s2, 0
	s_mov_b32 s3, 0
	s_barrier
; DI bf16x8 packS(const f32x16& x, int s) { return pack8(x[8 * s], x[8 * s + 1], x[8 * s + 2], x[8 * s + 3], x[8 * s + 4], x[8 * s + 5], x[8 * s + 6], x[8 * s + 7]); }
; DI void gdn_scan_seq(const Params& p, int bh16, char* ldsf) {
;     ...
;   for (int c = 0; c < 128; ++c) {
;     if (c + 1 < 128) asm volatile("s_waitcnt vmcnt(12)" ::: "memory"); else asm volatile("s_waitcnt vmcnt(0)" ::: "memory");
;     __builtin_amdgcn_s_barrier();
;     asm volatile("" ::: "memory");
;     char* sco = scp + (size_t)c * 32768;
;     bf16x8 Sb[4][2];
; #pragma unroll
;     for (int m = 0; m < 4; ++m) { Sb[m][0] = packS(S[m], 0); Sb[m][1] = packS(S[m], 1); *(bf16x8*)(sco + (m * 2 + 0) * 1024) = Sb[m][0]; *(bf16x8*)(sco + (m * 2 + 1) * 1024) = Sb[m][1]; }
;     __builtin_amdgcn_sched_barrier(0);
;     if (c + 2 < 128) { const int s2 = sl >= 1 ? sl - 1 : 2; SCAN_ISSUE(c + 2, s2); }
.Lshadow_loop:
	s_waitcnt vmcnt(36)
	v_add_u32_e32 v209, s3, v208
	v_add_u32_e32 v211, s3, v210
	ds_write_b128 v209, v[0:3]
	ds_write_b128 v209, v[4:7] offset:1024
	ds_write_b128 v209, v[8:11] offset:2048
	ds_write_b128 v209, v[12:15] offset:3072
	ds_write_b128 v209, v[16:19] offset:16384
	ds_write_b128 v209, v[20:23] offset:17408
	ds_write_b128 v209, v[24:27] offset:18432
	ds_write_b128 v209, v[28:31] offset:19456
	s_mov_b64 exec, s[16:17]
	ds_write_b128 v211, v[32:35] offset:32768
	ds_write_b128 v211, v[36:39] offset:33792
	ds_write_b128 v211, v[40:43] offset:34816
	ds_write_b128 v211, v[44:47] offset:35840
	s_mov_b64 exec, -1
	global_load_dwordx4 v[0:3], v132, s[8:9]
	global_load_dwordx4 v[4:7], v132, s[8:9] offset:1024
	global_load_dwordx4 v[8:11], v132, s[8:9] offset:2048
	global_load_dwordx4 v[12:15], v132, s[8:9] offset:3072
	global_load_dwordx4 v[16:19], v132, s[10:11]
	global_load_dwordx4 v[20:23], v132, s[10:11] offset:1024
	global_load_dwordx4 v[24:27], v132, s[10:11] offset:2048
	global_load_dwordx4 v[28:31], v132, s[10:11] offset:3072
	global_load_dwordx4 v[32:35], v133, s[12:13]
	global_load_dwordx4 v[36:39], v133, s[12:13] offset:16
	global_load_dwordx4 v[40:43], v134, s[12:13]
	global_load_dwordx4 v[44:47], v134, s[12:13] offset:16
	s_add_u32 s15, s15, 1
	s_cmp_lt_u32 s15, 0x80
	s_cselect_b32 s14, 0x4000, 0
	s_add_u32 s8, s8, s14
	s_addc_u32 s9, s9, 0
	s_add_u32 s10, s10, s14
	s_addc_u32 s11, s11, 0
	s_add_u32 s12, s12, s14
	s_addc_u32 s13, s13, 0
	s_xor_b32 s3, s3, 0xc000
	s_waitcnt lgkmcnt(0)
	s_barrier
	s_waitcnt vmcnt(36)
	v_add_u32_e32 v209, s3, v208
	v_add_u32_e32 v211, s3, v210
	ds_write_b128 v209, v[48:51]
	ds_write_b128 v209, v[52:55] offset:1024
	ds_write_b128 v209, v[56:59] offset:2048
	ds_write_b128 v209, v[60:63] offset:3072
	ds_write_b128 v209, v[64:67] offset:16384
	ds_write_b128 v209, v[68:71] offset:17408
	ds_write_b128 v209, v[72:75] offset:18432
	ds_write_b128 v209, v[76:79] offset:19456
	s_mov_b64 exec, s[16:17]
	ds_write_b128 v211, v[80:83] offset:32768
	ds_write_b128 v211, v[84:87] offset:33792
	ds_write_b128 v211, v[88:91] offset:34816
	ds_write_b128 v211, v[92:95] offset:35840
	s_mov_b64 exec, -1
	global_load_dwordx4 v[48:51], v132, s[8:9]
	global_load_dwordx4 v[52:55], v132, s[8:9] offset:1024
	global_load_dwordx4 v[56:59], v132, s[8:9] offset:2048
	global_load_dwordx4 v[60:63], v132, s[8:9] offset:3072
	global_load_dwordx4 v[64:67], v132, s[10:11]
	global_load_dwordx4 v[68:71], v132, s[10:11] offset:1024
	global_load_dwordx4 v[72:75], v132, s[10:11] offset:2048
	global_load_dwordx4 v[76:79], v132, s[10:11] offset:3072
	global_load_dwordx4 v[80:83], v133, s[12:13]
	global_load_dwordx4 v[84:87], v133, s[12:13] offset:16
	global_load_dwordx4 v[88:91], v134, s[12:13]
	global_load_dwordx4 v[92:95], v134, s[12:13] offset:16
	s_add_u32 s15, s15, 1
	s_cmp_lt_u32 s15, 0x80
	s_cselect_b32 s14, 0x4000, 0
	s_add_u32 s8, s8, s14
	s_addc_u32 s9, s9, 0
	s_add_u32 s10, s10, s14
	s_addc_u32 s11, s11, 0
	s_add_u32 s12, s12, s14
	s_addc_u32 s13, s13, 0
	s_xor_b32 s3, s3, 0xc000
	s_waitcnt lgkmcnt(0)
	s_barrier
	s_waitcnt vmcnt(36)
	v_add_u32_e32 v209, s3, v208
	v_add_u32_e32 v211, s3, v210
	ds_write_b128 v209, v[96:99]
	ds_write_b128 v209, v[100:103] offset:1024
	ds_write_b128 v209, v[104:107] offset:2048
	ds_write_b128 v209, v[108:111] offset:3072
	ds_write_b128 v209, v[112:115] offset:16384
	ds_write_b128 v209, v[116:119] offset:17408
	ds_write_b128 v209, v[120:123] offset:18432
	ds_write_b128 v209, v[124:127] offset:19456
	s_mov_b64 exec, s[16:17]
	ds_write_b128 v211, v[128:131] offset:32768
	ds_write_b128 v211, v[136:139] offset:33792
	ds_write_b128 v211, v[140:143] offset:34816
	ds_write_b128 v211, v[148:151] offset:35840
	s_mov_b64 exec, -1
	global_load_dwordx4 v[96:99], v132, s[8:9]
	global_load_dwordx4 v[100:103], v132, s[8:9] offset:1024
	global_load_dwordx4 v[104:107], v132, s[8:9] offset:2048
	global_load_dwordx4 v[108:111], v132, s[8:9] offset:3072
	global_load_dwordx4 v[112:115], v132, s[10:11]
	global_load_dwordx4 v[116:119], v132, s[10:11] offset:1024
	global_load_dwordx4 v[120:123], v132, s[10:11] offset:2048
	global_load_dwordx4 v[124:127], v132, s[10:11] offset:3072
	global_load_dwordx4 v[128:131], v133, s[12:13]
	global_load_dwordx4 v[136:139], v133, s[12:13] offset:16
	global_load_dwordx4 v[140:143], v134, s[12:13]
	global_load_dwordx4 v[148:151], v134, s[12:13] offset:16
	s_add_u32 s15, s15, 1
	s_cmp_lt_u32 s15, 0x80
	s_cselect_b32 s14, 0x4000, 0
	s_add_u32 s8, s8, s14
	s_addc_u32 s9, s9, 0
	s_add_u32 s10, s10, s14
	s_addc_u32 s11, s11, 0
	s_add_u32 s12, s12, s14
	s_addc_u32 s13, s13, 0
	s_xor_b32 s3, s3, 0xc000
	s_waitcnt lgkmcnt(0)
	s_barrier
	s_waitcnt vmcnt(36)
	v_add_u32_e32 v209, s3, v208
	v_add_u32_e32 v211, s3, v210
	ds_write_b128 v209, v[152:155]
	ds_write_b128 v209, v[156:159] offset:1024
	ds_write_b128 v209, v[160:163] offset:2048
	ds_write_b128 v209, v[164:167] offset:3072
	ds_write_b128 v209, v[168:171] offset:16384
	ds_write_b128 v209, v[172:175] offset:17408
	ds_write_b128 v209, v[178:181] offset:18432
	ds_write_b128 v209, v[182:185] offset:19456
	s_mov_b64 exec, s[16:17]
	ds_write_b128 v211, v[190:193] offset:32768
	ds_write_b128 v211, v[194:197] offset:33792
	ds_write_b128 v211, v[198:201] offset:34816
	ds_write_b128 v211, v[202:205] offset:35840
	s_mov_b64 exec, -1
	global_load_dwordx4 v[152:155], v132, s[8:9]
	global_load_dwordx4 v[156:159], v132, s[8:9] offset:1024
	global_load_dwordx4 v[160:163], v132, s[8:9] offset:2048
	global_load_dwordx4 v[164:167], v132, s[8:9] offset:3072
	global_load_dwordx4 v[168:171], v132, s[10:11]
	global_load_dwordx4 v[172:175], v132, s[10:11] offset:1024
	global_load_dwordx4 v[178:181], v132, s[10:11] offset:2048
	global_load_dwordx4 v[182:185], v132, s[10:11] offset:3072
	global_load_dwordx4 v[190:193], v133, s[12:13]
	global_load_dwordx4 v[194:197], v133, s[12:13] offset:16
	global_load_dwordx4 v[198:201], v134, s[12:13]
	global_load_dwordx4 v[202:205], v134, s[12:13] offset:16
	s_add_u32 s15, s15, 1
	s_cmp_lt_u32 s15, 0x80
	s_cselect_b32 s14, 0x4000, 0
	s_add_u32 s8, s8, s14
	s_addc_u32 s9, s9, 0
	s_add_u32 s10, s10, s14
	s_addc_u32 s11, s11, 0
	s_add_u32 s12, s12, s14
	s_addc_u32 s13, s13, 0
	s_xor_b32 s3, s3, 0xc000
	s_waitcnt lgkmcnt(0)
	s_barrier
	s_add_u32 s2, s2, 1
	s_cmp_lt_u32 s2, 32
	s_cbranch_scc1 .Lshadow_loop
	s_waitcnt vmcnt(0)
	s_barrier
; DI int tidx() { int t = threadIdx.x & 255; asm volatile("" : "+v"(t)); return t; }
; DI void gdn_scan_seq(const Params& p, int bh16, char* ldsf) {
;   const int tid = tidx(), lane = tid & 63, wv = tid >> 6;
;   const float* glp = (const float*)(p.ws + WS_GL) + bh16 * 128;
;   const char* wf = (const char*)(p.ws + WS_WF) + (size_t)bh16 * 128 * 16384 + tid * 16;
;   const char* kf = (const char*)p.out + 32 * MiB + (size_t)bh16 * 128 * 16384 + tid * 16;
;   const char* uf = (const char*)(p.ws + WS_UF) + (size_t)bh16 * 128 * 16384 + (size_t)(wv * 64 + lane) * 32;
;   char* scp = p.ws + WS_SC + (size_t)bh16 * 128 * 32768 + (size_t)wv * 8192 + lane * 16;
;   float* glt = (float*)(ldsf + 2 * LDS_BYTES + 64);
;   if (tid < 128) glt[tid] = glp[tid];
;     ...
;   f32x16 S[4];
; #pragma unroll
;   for (int m = 0; m < 4; ++m)
; #pragma unroll
;     for (int r = 0; r < 16; ++r) S[m][r] = 0.f;
;   asm volatile("s_waitcnt vmcnt(0)" ::: "memory");
;   __syncthreads();
;   SCAN_ISSUE(0, 0); SCAN_ISSUE(1, 1);
;   int sl = 0;
.LBB0_1212:
	s_andn2_saveexec_b64 s[2:3], s[6:7]
	s_cbranch_execz .LBB0_1226
	v_readlane_b32 s2, v250, 0
	v_lshrrev_b32_e32 v0, 6, v206
	v_and_b32_e32 v1, 63, v206
	v_lshlrev_b32_e32 v130, 4, v1
	v_readfirstlane_b32 s16, v206
	s_nop 3
	s_lshr_b32 s17, s2, 4
	s_and_b32 s2, s2, 15
	v_lshl_add_u32 v0, s17, 1, v0
	v_lshl_add_u32 v129, v0, 12, v130
	v_lshl_add_u32 v128, v0, 13, v130
	s_lshl_b32 s3, s2, 9
	s_add_u32 s12, s84, s3
	s_addc_u32 s13, s85, 0
	s_add_u32 s12, s12, 0x1a00000
	s_addc_u32 s13, s13, 0
	v_cmp_gt_u32_e32 vcc, 0x80, v206
	s_and_saveexec_b64 s[6:7], vcc
	s_cbranch_execz .Lscan_glt_done
	v_lshlrev_b32_e32 v2, 2, v206
	global_load_dword v3, v2, s[12:13]
	v_add_u32_e32 v2, 0x24040, v2
	s_waitcnt vmcnt(0)
	ds_write_b32 v2, v3
.Lscan_glt_done:
	s_or_b64 exec, exec, s[6:7]
	s_cmp_ge_u32 s16, 0x80
	s_cbranch_scc1 .Lscan_idle
	s_lshl_b32 s3, s2, 22
	s_add_u32 s8, s56, s3
	s_addc_u32 s9, s57, 0
	s_add_u32 s10, s8, 0x1000
	s_addc_u32 s11, s9, 0
	v_mov_b32_e32 v0, 0
	v_mov_b32_e32 v1, 0
	v_mov_b32_e32 v2, 0
	v_mov_b32_e32 v3, 0
	v_mov_b32_e32 v4, 0
	v_mov_b32_e32 v5, 0
	v_mov_b32_e32 v6, 0
	v_mov_b32_e32 v7, 0
	v_mov_b32_e32 v8, 0
	v_mov_b32_e32 v9, 0
	v_mov_b32_e32 v10, 0
	v_mov_b32_e32 v11, 0
	v_mov_b32_e32 v12, 0
	v_mov_b32_e32 v13, 0
	v_mov_b32_e32 v14, 0
	v_mov_b32_e32 v15, 0
	v_mov_b32_e32 v16, 0
	v_mov_b32_e32 v17, 0
	v_mov_b32_e32 v18, 0
	v_mov_b32_e32 v19, 0
	v_mov_b32_e32 v20, 0
	v_mov_b32_e32 v21, 0
	v_mov_b32_e32 v22, 0
	v_mov_b32_e32 v23, 0
	v_mov_b32_e32 v24, 0
	v_mov_b32_e32 v25, 0
	v_mov_b32_e32 v26, 0
	v_mov_b32_e32 v27, 0
	v_mov_b32_e32 v28, 0
	v_mov_b32_e32 v29, 0
	v_mov_b32_e32 v30, 0
	v_mov_b32_e32 v31, 0
	v_mov_b32_e32 v32, 0
	v_mov_b32_e32 v33, 0
	v_mov_b32_e32 v34, 0
	v_mov_b32_e32 v35, 0
	v_mov_b32_e32 v36, 0
	v_mov_b32_e32 v37, 0
	v_mov_b32_e32 v38, 0
	v_mov_b32_e32 v39, 0
	v_mov_b32_e32 v40, 0
	v_mov_b32_e32 v41, 0
	v_mov_b32_e32 v42, 0
	v_mov_b32_e32 v43, 0
	v_mov_b32_e32 v44, 0
	v_mov_b32_e32 v45, 0
	v_mov_b32_e32 v46, 0
	v_mov_b32_e32 v47, 0
	v_mov_b32_e32 v48, 0
	v_mov_b32_e32 v49, 0
	v_mov_b32_e32 v50, 0
	v_mov_b32_e32 v51, 0
	v_mov_b32_e32 v52, 0
	v_mov_b32_e32 v53, 0
	v_mov_b32_e32 v54, 0
	v_mov_b32_e32 v55, 0
	v_mov_b32_e32 v56, 0
	v_mov_b32_e32 v57, 0
	v_mov_b32_e32 v58, 0
	v_mov_b32_e32 v59, 0
	v_mov_b32_e32 v60, 0
	v_mov_b32_e32 v61, 0
	v_mov_b32_e32 v62, 0
	v_mov_b32_e32 v63, 0
	v_mov_b32_e32 v80, 0
	v_mov_b32_e32 v81, 0
	v_mov_b32_e32 v82, 0
	v_mov_b32_e32 v83, 0
	v_mov_b32_e32 v84, 0
	v_mov_b32_e32 v85, 0
	v_mov_b32_e32 v86, 0
	v_mov_b32_e32 v87, 0
	v_mov_b32_e32 v182, 0
	v_mov_b32_e32 v183, 0
	v_mov_b32_e32 v184, 0
	v_mov_b32_e32 v185, 0
	v_mov_b32_e32 v190, 0
	v_mov_b32_e32 v191, 0
	v_mov_b32_e32 v192, 0
	v_mov_b32_e32 v193, 0
	v_mov_b32_e32 v194, 0
	v_mov_b32_e32 v195, 0
	v_mov_b32_e32 v196, 0
	v_mov_b32_e32 v197, 0
	v_mov_b32_e32 v198, 0
	v_mov_b32_e32 v199, 0
	v_mov_b32_e32 v200, 0
	v_mov_b32_e32 v201, 0
	v_mov_b32_e32 v202, 0
	v_mov_b32_e32 v203, 0
	v_mov_b32_e32 v204, 0
	v_mov_b32_e32 v205, 0
	v_mov_b32_e32 v208, 0
	v_mov_b32_e32 v209, 0
	v_mov_b32_e32 v210, 0
	v_mov_b32_e32 v211, 0
	v_mov_b32_e32 v212, 0
	v_mov_b32_e32 v213, 0
	v_mov_b32_e32 v214, 0
	v_mov_b32_e32 v215, 0
	v_mov_b32_e32 v216, 0
	v_mov_b32_e32 v217, 0
	v_mov_b32_e32 v218, 0
	v_mov_b32_e32 v219, 0
	s_or_b32 s16, s16, s17
	s_lshl_b32 s3, s2, 6
	s_add_u32 s14, s84, s3
	s_addc_u32 s15, s85, 0
	s_add_u32 s14, s14, 0xc00
	s_addc_u32 s15, s15, 0
	v_mov_b32_e32 v132, 1
	v_mov_b32_e32 v133, 0
	s_mov_b32 s2, 0
	s_mov_b32 s3, 0
	s_mov_b32 s18, 0x24040
	s_waitcnt lgkmcnt(0)
	s_barrier

; DI float bflo(unsigned u) { return __uint_as_float(u << 16); }
; DI float bfhi(unsigned u) { return __uint_as_float(u & 0xffff0000u); }
; DI bf16x8 packS(const f32x16& x, int s) { return pack8(x[8 * s], x[8 * s + 1], x[8 * s + 2], x[8 * s + 3], x[8 * s + 4], x[8 * s + 5], x[8 * s + 6], x[8 * s + 7]); }
; #define SCAN_RDW(F, mh) do { _Pragma("unroll") for (int k = 0; k < 8; ++k) { const int i2 = k >> 2, m = 2 * (mh) + ((k >> 1) & 1), sx = k & 1; F[k] = *(const bf16x8*)(lw + ((i2 * 4 + m) * 2 + sx) * 1024); } } while (0)
; #define SCAN_RDK(F, mh) do { _Pragma("unroll") for (int k = 0; k < 8; ++k) { const int m = 2 * (mh) + (k >> 2), j2 = (k >> 1) & 1, sx = k & 1; F[k] = *(const bf16x8*)(lk + ((m * 2 + j2) * 2 + sx) * 1024); } } while (0)
; #define SCAN_MMW(F, mh) do { _Pragma("unroll") for (int q = 0; q < 4; ++q) { const int m = 2 * (mh) + (q >> 1), sx = q & 1; vn[0] = MFMA32(F[q], Sb[m][sx], vn[0]); vn[1] = MFMA32(F[4 + q], Sb[m][sx], vn[1]); } } while (0)
; DI void gdn_scan_seq(const Params& p, int bh16, char* ldsf) {
;     ...
;     bf16x8 Sb[4][2];
; #pragma unroll
;     for (int m = 0; m < 4; ++m) { Sb[m][0] = packS(S[m], 0); Sb[m][1] = packS(S[m], 1); *(bf16x8*)(sco + (m * 2 + 0) * 1024) = Sb[m][0]; *(bf16x8*)(sco + (m * 2 + 1) * 1024) = Sb[m][1]; }
;     __builtin_amdgcn_sched_barrier(0);
;     if (c + 2 < 128) { const int s2 = sl >= 1 ? sl - 1 : 2; SCAN_ISSUE(c + 2, s2); }
;     const char* base = ldsf + sl * 49152;
;     const char* lw = base + lane * 16; const char* lk = lw + 16384; const char* lu = base + 32768 + wv * 4096 + lane * 16;
;     const float gl = glt[c];
;     f32x16 vn[2];
; #pragma unroll
;     for (int i2 = 0; i2 < 2; ++i2) {
;       const u32x4 ua = *(const u32x4*)(lu + (2 * i2) * 1024), ub = *(const u32x4*)(lu + (2 * i2 + 1) * 1024);
; #pragma unroll
;       for (int e = 0; e < 4; ++e) { vn[i2][2 * e] = bflo(ua[e]); vn[i2][2 * e + 1] = bfhi(ua[e]); vn[i2][8 + 2 * e] = bflo(ub[e]); vn[i2][8 + 2 * e + 1] = bfhi(ub[e]); }
;     }
;     bf16x8 fa[8], fb[8];
;     ...
;     SCAN_RDW(fa, 0);
;     __builtin_amdgcn_sched_barrier(0);
;     SCAN_RDW(fb, 1);
;     __builtin_amdgcn_sched_barrier(0);
;     SCAN_MMW(fa, 0);
;     __builtin_amdgcn_sched_barrier(0);
;     SCAN_RDK(fa, 0);
.Lscan_noprog:
	v_add_u32_e32 v131, s3, v130
	v_add_u32_e32 v134, s3, v129
	v_mov_b32_e32 v143, s18
	ds_read_b128 v[72:75], v134 offset:32768
	ds_read_b128 v[76:79], v134 offset:33792
	ds_read_b32 v142, v143
	ds_read_b128 v[148:151], v131 offset:0
	ds_read_b128 v[152:155], v131 offset:1024
	ds_read_b128 v[156:159], v131 offset:2048
	ds_read_b128 v[160:163], v131 offset:3072
	ds_read_b128 v[164:167], v131 offset:4096
	ds_read_b128 v[168:171], v131 offset:5120
	ds_read_b128 v[172:175], v131 offset:6144
	ds_read_b128 v[178:181], v131 offset:7168
	ds_read_b128 v[88:91], v134 offset:34816
	ds_read_b128 v[92:95], v134 offset:35840
	s_waitcnt lgkmcnt(10)
	v_mfma_f32_32x32x16_bf16 v[0:15], v[182:185], v[80:83], v[0:15]
	v_lshlrev_b32_e32 v64, 16, v72
	v_and_b32_e32 v65, 0xffff0000, v72
	v_lshlrev_b32_e32 v66, 16, v73
	v_and_b32_e32 v67, 0xffff0000, v73
	v_mfma_f32_32x32x16_bf16 v[0:15], v[190:193], v[84:87], v[0:15]
	v_lshlrev_b32_e32 v68, 16, v74
	v_and_b32_e32 v69, 0xffff0000, v74
	v_lshlrev_b32_e32 v70, 16, v75
	v_and_b32_e32 v71, 0xffff0000, v75
	v_mfma_f32_32x32x16_bf16 v[16:31], v[194:197], v[80:83], v[16:31]
	v_lshlrev_b32_e32 v72, 16, v76
	v_and_b32_e32 v73, 0xffff0000, v76
	v_lshlrev_b32_e32 v74, 16, v77
	v_and_b32_e32 v75, 0xffff0000, v77
	v_mfma_f32_32x32x16_bf16 v[16:31], v[198:201], v[84:87], v[16:31]
	v_lshlrev_b32_e32 v76, 16, v78
	v_and_b32_e32 v77, 0xffff0000, v78
	v_lshlrev_b32_e32 v78, 16, v79
	v_and_b32_e32 v79, 0xffff0000, v79
	v_mfma_f32_32x32x16_bf16 v[32:47], v[202:205], v[80:83], v[32:47]
	v_cvt_pk_bf16_f32 v96, v0, v1
	v_cvt_pk_bf16_f32 v97, v2, v3
	v_cvt_pk_bf16_f32 v98, v4, v5
	v_cvt_pk_bf16_f32 v99, v6, v7
	v_cvt_pk_bf16_f32 v100, v8, v9
	v_mfma_f32_32x32x16_bf16 v[32:47], v[208:211], v[84:87], v[32:47]
	v_cvt_pk_bf16_f32 v101, v10, v11
	v_cvt_pk_bf16_f32 v102, v12, v13
	v_cvt_pk_bf16_f32 v103, v14, v15
	v_mfma_f32_32x32x16_bf16 v[48:63], v[212:215], v[80:83], v[48:63]
	v_cvt_pk_bf16_f32 v104, v16, v17
	v_cvt_pk_bf16_f32 v105, v18, v19
	v_cvt_pk_bf16_f32 v106, v20, v21
	v_cvt_pk_bf16_f32 v107, v22, v23
	v_cvt_pk_bf16_f32 v108, v24, v25
	v_mfma_f32_32x32x16_bf16 v[48:63], v[216:219], v[84:87], v[48:63]
	v_cvt_pk_bf16_f32 v109, v26, v27
	v_cvt_pk_bf16_f32 v110, v28, v29
	v_cvt_pk_bf16_f32 v111, v30, v31
	s_waitcnt lgkmcnt(0)
	ds_read_b128 v[182:185], v131 offset:8192
	ds_read_b128 v[190:193], v131 offset:9216
	ds_read_b128 v[194:197], v131 offset:10240
	ds_read_b128 v[198:201], v131 offset:11264
	ds_read_b128 v[202:205], v131 offset:12288
	ds_read_b128 v[208:211], v131 offset:13312
	ds_read_b128 v[212:215], v131 offset:14336
	ds_read_b128 v[216:219], v131 offset:15360
	v_mfma_f32_32x32x16_bf16 v[64:79], v[148:151], v[96:99], v[64:79]
	v_cvt_pk_bf16_f32 v112, v32, v33
	v_cvt_pk_bf16_f32 v113, v34, v35
	v_cvt_pk_bf16_f32 v114, v36, v37
	v_cvt_pk_bf16_f32 v115, v38, v39
	v_lshlrev_b32_e32 v80, 16, v88
	v_mfma_f32_32x32x16_bf16 v[64:79], v[152:155], v[100:103], v[64:79]
	v_cvt_pk_bf16_f32 v116, v40, v41
	v_cvt_pk_bf16_f32 v117, v42, v43
	v_cvt_pk_bf16_f32 v118, v44, v45
	v_cvt_pk_bf16_f32 v119, v46, v47
	v_and_b32_e32 v81, 0xffff0000, v88
	v_mfma_f32_32x32x16_bf16 v[64:79], v[156:159], v[104:107], v[64:79]
	v_cvt_pk_bf16_f32 v120, v48, v49
	v_cvt_pk_bf16_f32 v121, v50, v51
	v_cvt_pk_bf16_f32 v122, v52, v53
	v_cvt_pk_bf16_f32 v123, v54, v55
	v_lshlrev_b32_e32 v82, 16, v89
	v_mfma_f32_32x32x16_bf16 v[64:79], v[160:163], v[108:111], v[64:79]
	v_cvt_pk_bf16_f32 v124, v56, v57
	v_cvt_pk_bf16_f32 v125, v58, v59
	v_cvt_pk_bf16_f32 v126, v60, v61
	v_cvt_pk_bf16_f32 v127, v62, v63
	v_and_b32_e32 v83, 0xffff0000, v89
	global_store_dwordx4 v128, v[96:99], s[8:9]
	v_mfma_f32_32x32x16_bf16 v[64:79], v[164:167], v[112:115], v[64:79]
	v_lshlrev_b32_e32 v84, 16, v90
	v_and_b32_e32 v85, 0xffff0000, v90
	v_lshlrev_b32_e32 v86, 16, v91
	v_and_b32_e32 v87, 0xffff0000, v91
	v_lshlrev_b32_e32 v88, 16, v92
	global_store_dwordx4 v128, v[100:103], s[8:9] offset:1024
	v_mfma_f32_32x32x16_bf16 v[64:79], v[168:171], v[116:119], v[64:79]
	v_and_b32_e32 v89, 0xffff0000, v92
	v_lshlrev_b32_e32 v90, 16, v93
	v_and_b32_e32 v91, 0xffff0000, v93
	v_lshlrev_b32_e32 v92, 16, v94
	v_and_b32_e32 v93, 0xffff0000, v94
	global_store_dwordx4 v128, v[104:107], s[8:9] offset:2048
	v_mfma_f32_32x32x16_bf16 v[64:79], v[172:175], v[120:123], v[64:79]
	v_lshlrev_b32_e32 v94, 16, v95
	v_and_b32_e32 v95, 0xffff0000, v95
	global_store_dwordx4 v128, v[108:111], s[8:9] offset:3072
	v_mul_f32_e32 v0, v142, v0
	v_mul_f32_e32 v1, v142, v1
	v_mfma_f32_32x32x16_bf16 v[64:79], v[178:181], v[124:127], v[64:79]
	v_mul_f32_e32 v2, v142, v2
	v_mul_f32_e32 v3, v142, v3
	v_mul_f32_e32 v4, v142, v4
	v_mul_f32_e32 v5, v142, v5
	v_mul_f32_e32 v6, v142, v6
	s_waitcnt lgkmcnt(0)
; DI bf16x8 packS(const f32x16& x, int s) { return pack8(x[8 * s], x[8 * s + 1], x[8 * s + 2], x[8 * s + 3], x[8 * s + 4], x[8 * s + 5], x[8 * s + 6], x[8 * s + 7]); }
; #define SCAN_RDK(F, mh) do { _Pragma("unroll") for (int k = 0; k < 8; ++k) { const int m = 2 * (mh) + (k >> 2), j2 = (k >> 1) & 1, sx = k & 1; F[k] = *(const bf16x8*)(lk + ((m * 2 + j2) * 2 + sx) * 1024); } } while (0)
; #define SCAN_MMW(F, mh) do { _Pragma("unroll") for (int q = 0; q < 4; ++q) { const int m = 2 * (mh) + (q >> 1), sx = q & 1; vn[0] = MFMA32(F[q], Sb[m][sx], vn[0]); vn[1] = MFMA32(F[4 + q], Sb[m][sx], vn[1]); } } while (0)
; #define SCAN_MMK(F, mh) do { _Pragma("unroll") for (int q = 0; q < 4; ++q) { const int j2 = q >> 1, sx = q & 1; S[2 * (mh)] = MFMA32(F[q], Vb[j2][sx], S[2 * (mh)]); S[2 * (mh) + 1] = MFMA32(F[4 + q], Vb[j2][sx], S[2 * (mh) + 1]); } } while (0)
; DI void gdn_scan_seq(const Params& p, int bh16, char* ldsf) {
;     ...
;     SCAN_MMW(fb, 1);
;     __builtin_amdgcn_sched_barrier(0);
;     SCAN_RDK(fb, 1);
;     __builtin_amdgcn_sched_barrier(0);
;     bf16x8 Vb[2][2];
; #pragma unroll
;     for (int j2 = 0; j2 < 2; ++j2) { Vb[j2][0] = packS(vn[j2], 0); Vb[j2][1] = packS(vn[j2], 1); }
; #pragma unroll
;     for (int m = 0; m < 4; ++m)
; #pragma unroll
;       for (int r = 0; r < 16; ++r) S[m][r] *= gl;
;     SCAN_MMK(fa, 0);
;     SCAN_MMK(fb, 1);
;     ...
;     asm volatile("s_waitcnt lgkmcnt(0)" ::: "memory");
;     sl = sl == 2 ? 0 : sl + 1;
;   }
; DI void phase_mixer(const Params& p, int bid, int nb, char* lds, char* ctl, char* ldsf) {
;     ...
;   if (bid < 32) { if (vb == 0) gdn_scan_seq(p, bid >> 1, ldsf); else { __syncthreads(); for (int k = 0; k < 128; ++k) { __builtin_amdgcn_s_barrier(); asm volatile("" ::: "memory"); } __syncthreads(); } }
	ds_read_b128 v[148:151], v131 offset:16384
	ds_read_b128 v[152:155], v131 offset:17408
	ds_read_b128 v[156:159], v131 offset:20480
	ds_read_b128 v[160:163], v131 offset:21504
	ds_read_b128 v[164:167], v131 offset:24576
	ds_read_b128 v[168:171], v131 offset:25600
	ds_read_b128 v[172:175], v131 offset:28672
	ds_read_b128 v[178:181], v131 offset:29696
	v_mfma_f32_32x32x16_bf16 v[80:95], v[182:185], v[96:99], v[80:95]
	v_mul_f32_e32 v7, v142, v7
	v_mul_f32_e32 v8, v142, v8
	v_mul_f32_e32 v9, v142, v9
	v_mul_f32_e32 v10, v142, v10
	v_mul_f32_e32 v11, v142, v11
	v_mfma_f32_32x32x16_bf16 v[80:95], v[190:193], v[100:103], v[80:95]
	v_mul_f32_e32 v12, v142, v12
	v_mul_f32_e32 v13, v142, v13
	v_mul_f32_e32 v14, v142, v14
	v_mul_f32_e32 v15, v142, v15
	global_store_dwordx4 v128, v[112:115], s[10:11]
	v_mfma_f32_32x32x16_bf16 v[80:95], v[194:197], v[104:107], v[80:95]
	v_mul_f32_e32 v16, v142, v16
	v_mul_f32_e32 v17, v142, v17
	v_mul_f32_e32 v18, v142, v18
	v_mul_f32_e32 v19, v142, v19
	global_store_dwordx4 v128, v[116:119], s[10:11] offset:1024
	v_mul_f32_e32 v32, v142, v32
	v_mfma_f32_32x32x16_bf16 v[80:95], v[198:201], v[108:111], v[80:95]
	v_mul_f32_e32 v20, v142, v20
	v_mul_f32_e32 v21, v142, v21
	v_mul_f32_e32 v22, v142, v22
	v_mul_f32_e32 v23, v142, v23
	global_store_dwordx4 v128, v[120:123], s[10:11] offset:2048
	v_mul_f32_e32 v33, v142, v33
	v_mfma_f32_32x32x16_bf16 v[80:95], v[202:205], v[112:115], v[80:95]
	v_mul_f32_e32 v24, v142, v24
	v_mul_f32_e32 v25, v142, v25
	v_mul_f32_e32 v26, v142, v26
	v_mul_f32_e32 v27, v142, v27
	global_store_dwordx4 v128, v[124:127], s[10:11] offset:3072
	v_mul_f32_e32 v34, v142, v34
	v_mfma_f32_32x32x16_bf16 v[80:95], v[208:211], v[116:119], v[80:95]
	v_mul_f32_e32 v28, v142, v28
	v_mul_f32_e32 v29, v142, v29
	v_mul_f32_e32 v30, v142, v30
	v_mul_f32_e32 v31, v142, v31
	v_cvt_pk_bf16_f32 v64, v64, v65
	v_mul_f32_e32 v35, v142, v35
	v_mfma_f32_32x32x16_bf16 v[80:95], v[212:215], v[120:123], v[80:95]
	v_cvt_pk_bf16_f32 v65, v66, v67
	v_cvt_pk_bf16_f32 v66, v68, v69
	v_cvt_pk_bf16_f32 v67, v70, v71
	v_cvt_pk_bf16_f32 v68, v72, v73
	v_cvt_pk_bf16_f32 v69, v74, v75
	v_mul_f32_e32 v36, v142, v36
	v_mfma_f32_32x32x16_bf16 v[80:95], v[216:219], v[124:127], v[80:95]
	v_cvt_pk_bf16_f32 v70, v76, v77
	v_cvt_pk_bf16_f32 v71, v78, v79
	v_mul_f32_e32 v37, v142, v37
	v_mul_f32_e32 v38, v142, v38
	v_mul_f32_e32 v39, v142, v39
	v_mul_f32_e32 v40, v142, v40
	s_waitcnt lgkmcnt(0)
	ds_read_b128 v[182:185], v131 offset:18432
	ds_read_b128 v[190:193], v131 offset:19456
	ds_read_b128 v[194:197], v131 offset:22528
	ds_read_b128 v[198:201], v131 offset:23552
	ds_read_b128 v[202:205], v131 offset:26624
	ds_read_b128 v[208:211], v131 offset:27648
	ds_read_b128 v[212:215], v131 offset:30720
	ds_read_b128 v[216:219], v131 offset:31744
	v_mfma_f32_32x32x16_bf16 v[0:15], v[148:151], v[64:67], v[0:15]
	v_mul_f32_e32 v41, v142, v41
	v_mul_f32_e32 v42, v142, v42
	v_mul_f32_e32 v43, v142, v43
	v_mul_f32_e32 v44, v142, v44
	v_mul_f32_e32 v45, v142, v45
	v_mul_f32_e32 v46, v142, v46
	s_add_u32 s2, s2, 1
	s_xor_b32 s3, s3, 0xc000
	s_add_u32 s18, s18, 4
	s_add_u32 s8, s8, 0x8000
	s_addc_u32 s9, s9, 0
	s_add_u32 s10, s10, 0x8000
	s_addc_u32 s11, s11, 0
	v_mfma_f32_32x32x16_bf16 v[0:15], v[152:155], v[68:71], v[0:15]
	v_mul_f32_e32 v47, v142, v47
	v_mul_f32_e32 v48, v142, v48
	v_mul_f32_e32 v49, v142, v49
	v_mul_f32_e32 v50, v142, v50
	v_mul_f32_e32 v51, v142, v51
	v_mul_f32_e32 v52, v142, v52
	v_mfma_f32_32x32x16_bf16 v[16:31], v[156:159], v[64:67], v[16:31]
	v_mul_f32_e32 v53, v142, v53
	v_mul_f32_e32 v54, v142, v54
	v_mul_f32_e32 v55, v142, v55
	v_mul_f32_e32 v56, v142, v56
	v_mul_f32_e32 v57, v142, v57
	v_mul_f32_e32 v58, v142, v58
	v_mfma_f32_32x32x16_bf16 v[16:31], v[160:163], v[68:71], v[16:31]
	v_mul_f32_e32 v59, v142, v59
	v_mul_f32_e32 v60, v142, v60
	v_mul_f32_e32 v61, v142, v61
	v_mul_f32_e32 v62, v142, v62
	v_mul_f32_e32 v63, v142, v63
	v_cvt_pk_bf16_f32 v80, v80, v81
	v_mfma_f32_32x32x16_bf16 v[32:47], v[164:167], v[64:67], v[32:47]
	v_cvt_pk_bf16_f32 v81, v82, v83
	v_cvt_pk_bf16_f32 v82, v84, v85
	v_cvt_pk_bf16_f32 v83, v86, v87
	v_cvt_pk_bf16_f32 v84, v88, v89
	v_cvt_pk_bf16_f32 v85, v90, v91
	v_cvt_pk_bf16_f32 v86, v92, v93
	v_mfma_f32_32x32x16_bf16 v[32:47], v[168:171], v[68:71], v[32:47]
	v_cvt_pk_bf16_f32 v87, v94, v95
	v_mfma_f32_32x32x16_bf16 v[48:63], v[172:175], v[64:67], v[48:63]
	v_mfma_f32_32x32x16_bf16 v[48:63], v[178:181], v[68:71], v[48:63]
	s_cmp_lt_u32 s2, 0x80
	s_waitcnt lgkmcnt(0)
	s_cbranch_scc1 .Lscan_loop
	s_branch .Lscan_end
.Lscan_idle:
	s_mov_b32 s2, 0
	s_barrier
.Lscan_idle_loop:
	s_barrier
	s_add_u32 s2, s2, 1
	s_cmp_lt_u32 s2, 0x80
	s_cbranch_scc1 .Lscan_idle_loop

; #define LAS __attribute__((address_space(3)))
; DI int tidx() { int t = threadIdx.x & 255; asm volatile("" : "+v"(t)); return t; }
; DI void phase_mixer(const Params& p, int bid, int nb, char* lds, char* ctl, char* ldsf) {
;   const int vb = threadIdx.x >> 8, lane = tidx() & 63;
;   if (bid < 32) { if (vb == 0) gdn_scan_seq(p, bid >> 1, ldsf); else { __syncthreads(); for (int k = 0; k < 128; ++k) { __builtin_amdgcn_s_barrier(); asm volatile("" ::: "memory"); } __syncthreads(); } }
;   unsigned* ctr = (unsigned*)(p.ws + WS_CTL);
;   volatile LAS int* slot = (volatile LAS int*)(ctl + 16 + 4 * vb);
;   volatile LAS unsigned* hbc = (volatile LAS unsigned*)(ctl + 32 + 4 * vb);
;   unsigned hbph = 0u;
.LBB0_1226:
.LBB0_1227:
	s_or_b64 exec, exec, s[0:1]
	v_readlane_b32 s2, v250, 0
	v_readfirstlane_b32 s3, v207
	s_nop 3
	s_sub_u32 s14, s2, 32
	s_cmp_lt_u32 s14, 32
	s_cbranch_scc0 .Lpf_done
	s_and_b32 s15, s3, 0xff
	s_cmp_eq_u32 s15, 0
	s_cbranch_scc0 .Lpf_done
	s_lshr_b32 s24, s14, 3
	s_and_b32 s14, s14, 7
	s_lshr_b32 s15, s3, 8
	s_lshl_b32 s15, s15, 3
	s_add_u32 s14, s14, s15
	s_lshl_b32 s15, s14, 21
	s_lshl_b32 s3, s24, 14
	s_add_u32 s15, s15, s3
	s_add_u32 s16, s84, s15
	s_addc_u32 s17, s85, 0
	s_add_u32 s18, s16, 0x1c000000
	s_addc_u32 s19, s17, 0
	s_add_u32 s16, s16, 0x1e000000
	s_addc_u32 s17, s17, 0
	s_add_u32 s22, s66, s15
	s_addc_u32 s23, s67, 0
	s_add_u32 s22, s22, 0x2000000
	s_addc_u32 s23, s23, 0
	s_lshl_b32 s15, s14, 6
	s_add_u32 s2, s84, s15
	s_addc_u32 s3, s85, 0
	s_add_u32 s2, s2, 0xc00
	s_addc_u32 s3, s3, 0
	v_mbcnt_lo_u32_b32 v0, -1, 0
	v_mbcnt_hi_u32_b32 v0, -1, v0
	v_lshlrev_b32_e32 v0, 7, v0
	v_add_u32_e32 v111, 0x2000, v0
	v_mov_b32_e32 v1, 0
	s_mov_b32 s14, s24
	s_mov_b32 s24, 0
